# attention sb/fox inner loops: packed f32 VALU ops (v_pk_mul/add_f32) split into scalar ops, dead halves dropped (guide 7.5)
# speedup vs baseline: 1.0116x; 1.0116x over previous
; #define ATT_PACK8(P, B) __builtin_bit_cast(bf16x8, (v4u){cvtpk(P[B], P[B + 1]), cvtpk(P[B + 2], P[B + 3]), cvtpk(P[B + 4], P[B + 5]), cvtpk(P[B + 6], P[B + 7])})
; #define DILP_STORE() do { _Pragma("unroll") for (int i = 0; i < 4; ++i) { const int id = lane + 64 * i, key = id >> 3, ch = id & 7; \
;         *(LAS v4u*)(wl + ch * 512 + ((key ^ ch) << 4)) = kreg[i]; *(LAS v4u*)(wl + 4096 + (ch >> 2) * 2048 + ((key ^ (ch >> 2)) << 6) + (ch & 3) * 16) = vreg[i]; } } while (0)
; __device__ __forceinline__ void sb_wave_unit(const bf16* proj, const float* gn, unsigned char* obuf, int b, int h, int qt, lptr wl, LAS float* wsf, int lane) {
;     ...
;     for (;;) {
;         DILP_STORE();
;         const int kv0 = 32 * tt + 4 * hi; const bool diag = (tt == qt), more = tt > 0;
;         if (more) { DILP_LOAD(0, 0, tt - 1); }
;         f32x16 p0; qk32(p0, qr, wl, r32, hi);
;         asm volatile("s_nop 15\n\ts_nop 7" : "+v"(p0));
;         float run = 1.f;
; #pragma unroll
;         for (int j = 3; j >= 0; --j) {
;             float kk[4], bb[4];
; #pragma unroll
;             for (int e = 0; e < 4; ++e) { float yc; asm("v_min_f32_e32 %0, 0x42a00000, %1" : "=v"(yc) : "v"(p0[4 * j + e])); const float ex = __builtin_amdgcn_exp2f(yc); kk[e] = __builtin_amdgcn_rcpf(1.0f + ex); bb[e] = ex * kk[e];
;                 if (diag) { const int kv = kv0 + 8 * j + e; if (kv >= qtok) { kk[e] = 1.f; bb[e] = 0.f; } } }
;             const float s2 = kk[3], s1 = kk[3] * kk[2], s0 = s1 * kk[1], Gp = s0 * kk[0];
;             auto rr = __builtin_amdgcn_permlane32_swap(__float_as_uint(Gp), __float_as_uint(Gp), false, false);
;             const float ga = __uint_as_float(rr[0]), gb = __uint_as_float(rr[1]);
;             const float after = R * run * (hi ? 1.0f : gb);
;             p0[4 * j] = bb[0] * after * s0; p0[4 * j + 1] = bb[1] * after * s1; p0[4 * j + 2] = bb[2] * after * s2; p0[4 * j + 3] = bb[3] * after;
;             run *= ga * gb;
;         }
;         R *= run;
;         const bf16x8 pa0 = ATT_PACK8(p0, 0), pa1 = ATT_PACK8(p0, 8);
;         pv_step<2048>(o, wl + vbo, vsw, 0, pa0); pv_step<2048>(o, wl + vbo, vsw, 1, pa1);
;         if (!more || !__any(R >= 1e-30f)) break;
;     ...
;     }
.LBB0_392:
	ds_read_b128 v[32:35], v145 offset:57344
	ds_read_b128 v[180:183], v146 offset:57344
	s_andn2_b64 vcc, exec, s[10:11]
	s_waitcnt lgkmcnt(1)
	v_mfma_f32_32x32x16_bf16 v[32:47], v[32:35], v[48:51], 0
	s_waitcnt lgkmcnt(0)
	v_mfma_f32_32x32x16_bf16 v[32:47], v[180:183], v[52:55], v[32:47]
	ds_read_b128 v[180:183], v147 offset:57344
	ds_read_b128 v[184:187], v152 offset:57344
	s_waitcnt lgkmcnt(1)
	v_mfma_f32_32x32x16_bf16 v[32:47], v[180:183], v[56:59], v[32:47]
	s_waitcnt lgkmcnt(0)
	v_mfma_f32_32x32x16_bf16 v[32:47], v[184:187], v[60:63], v[32:47]
	s_nop 15
	s_nop 7
	s_nop 0
	v_min_f32_e32 v45, 0x42a00000, v45
	v_min_f32_e32 v46, 0x42a00000, v46
	v_min_f32_e32 v47, 0x42a00000, v47
	v_min_f32_e32 v180, 0x42a00000, v41
	v_min_f32_e32 v44, 0x42a00000, v44
	v_min_f32_e32 v181, 0x42a00000, v42
	s_nop 10
	v_exp_f32_e32 v102, v45
	v_exp_f32_e32 v45, v46
	v_exp_f32_e32 v41, v47
	v_exp_f32_e32 v183, v44
	v_min_f32_e32 v43, 0x42a00000, v43
	v_min_f32_e32 v40, 0x42a00000, v40
	v_exp_f32_e32 v42, v180
	v_exp_f32_e32 v46, v40
	v_exp_f32_e32 v181, v181
	v_exp_f32_e32 v43, v43
	v_add_f32_e32 v47, 1.0, v45
	v_add_f32_e32 v180, 1.0, v41
	v_add_f32_e32 v44, 1.0, v102
	v_rcp_f32_e32 v187, v47
	v_rcp_f32_e32 v47, v180
	v_add_f32_e32 v40, 1.0, v183
	v_rcp_f32_e32 v44, v44
	v_rcp_f32_e32 v189, v40
	v_add_f32_e32 v182, 1.0, v46
	v_add_f32_e32 v184, 1.0, v42
	v_add_f32_e32 v185, 1.0, v181
	v_add_f32_e32 v186, 1.0, v43
	v_rcp_f32_e32 v191, v182
	v_rcp_f32_e32 v180, v184
	v_rcp_f32_e32 v184, v185
	v_rcp_f32_e32 v182, v186
	v_mul_f32_e32 v185, v187, v47
	v_mul_f32_e32 v188, v44, v185
	v_mul_f32_e32 v192, v189, v188
	v_mov_b32_e32 v194, v192
	v_min_f32_e32 v36, 0x42a00000, v36
	v_mul_f32_e32 v40, v45, v187
	v_mul_f32_e32 v187, v184, v182
	v_permlane32_swap_b32_e32 v192, v194
	v_exp_f32_e32 v36, v36
	v_mul_f32_e32 v190, v180, v187
	v_cndmask_b32_e64 v45, 1.0, v194, s[6:7]
	v_mul_f32_e32 v193, v191, v190
	v_mul_f32_e32 v44, v102, v44
	v_mul_f32_e32 v45, v103, v45
	v_mul_f32_e32 v198, v46, v191
	v_mov_b32_e32 v195, v193
	v_mov_b32_e32 v46, v45
	s_nop 0
	v_permlane32_swap_b32_e32 v193, v195
	v_mul_f32_e32 v197, v44, v45
	v_mul_f32_e32 v40, v40, v46
	v_mul_f32_e32 v41, v41, v47
	v_add_f32_e32 v44, 1.0, v36
	v_mul_f32_e32 v186, v183, v189
	v_mov_b32_e32 v189, v197
	v_mul_f32_e32 v196, v47, v40
	v_mul_f32_e32 v197, v46, v41
	v_mul_f32_e32 v40, v192, v194
	v_mul_f32_e32 v41, v193, v195
	v_rcp_f32_e32 v46, v44
	v_mul_f32_e32 v199, v181, v184
	v_mul_f32_e32 v183, v43, v182
	v_mul_f32_e32 v43, v103, v40
	v_cndmask_b32_e64 v181, 1.0, v195, s[6:7]
	v_mul_f32_e32 v180, v42, v180
	v_mul_f32_e32 v181, v43, v181
	v_mul_f32_e32 v184, v186, v45
	v_mul_f32_e32 v45, v180, v181
	v_mul_f32_e32 v44, v36, v46
	v_min_f32_e32 v36, 0x42a00000, v37
	v_min_f32_e32 v37, 0x42a00000, v38
	v_min_f32_e32 v38, 0x42a00000, v39
	v_mul_f32_e32 v188, v184, v188
	v_mul_f32_e32 v189, v185, v189
	v_exp_f32_e32 v37, v37
	v_exp_f32_e32 v39, v38
	v_exp_f32_e32 v36, v36
	v_mov_b32_e32 v192, v40
	v_add_f32_e32 v38, 1.0, v37
	v_rcp_f32_e32 v43, v38
	v_add_f32_e32 v38, 1.0, v39
	v_rcp_f32_e32 v38, v38
	v_add_f32_e32 v42, 1.0, v36
	v_rcp_f32_e32 v42, v42
	v_mov_b32_e32 v194, v41
	v_mul_f32_e32 v47, v43, v38
	v_mul_f32_e32 v102, v37, v43
	v_mul_f32_e32 v184, v42, v47
	v_mul_f32_e32 v193, v46, v184
	v_mov_b32_e32 v195, v193
	s_nop 1
	v_permlane32_swap_b32_e32 v193, v195
	v_mul_f32_e32 v40, v192, v194
	v_mul_f32_e32 v41, v193, v195
	v_cndmask_b32_e64 v43, 1.0, v195, s[6:7]
	v_mul_f32_e32 v37, v103, v40
	v_mul_f32_e32 v36, v36, v42
	v_mul_f32_e32 v37, v37, v43
	v_min_f32_e32 v34, 0x42a00000, v34
	v_min_f32_e32 v35, 0x42a00000, v35
	v_mul_f32_e32 v39, v39, v38
	v_mul_f32_e32 v43, v36, v37
	v_mul_f32_e32 v46, v44, v37
	v_mov_b32_e32 v185, v43
	v_mul_f32_e32 v36, v102, v37
	v_exp_f32_e32 v34, v34
	v_exp_f32_e32 v35, v35
	v_min_f32_e32 v32, 0x42a00000, v32
	v_mul_f32_e32 v42, v46, v184
	v_mul_f32_e32 v43, v47, v185
	v_exp_f32_e32 v44, v32
	v_mul_f32_e32 v46, v38, v36
	v_mul_f32_e32 v47, v39, v37
	v_min_f32_e32 v33, 0x42a00000, v33
	v_add_f32_e32 v37, 1.0, v35
	v_exp_f32_e32 v36, v33
	v_add_f32_e32 v33, 1.0, v34
	v_add_f32_e32 v32, 1.0, v44
	v_rcp_f32_e32 v33, v33
	v_rcp_f32_e32 v38, v37
	v_add_f32_e32 v37, 1.0, v36
	v_rcp_f32_e32 v180, v32
	v_mul_f32_e32 v32, v40, v41
	v_rcp_f32_e32 v40, v37
	v_mul_f32_e32 v185, v33, v38
	v_mul_f32_e32 v102, v34, v33
	v_mul_f32_e32 v37, v103, v32
	v_mul_f32_e32 v192, v40, v185
	v_mul_f32_e32 v33, v180, v192
	v_mov_b32_e32 v34, v33
	s_nop 1
	v_permlane32_swap_b32_e32 v33, v34
	v_cndmask_b32_e64 v41, 1.0, v34, s[6:7]
	v_mul_f32_e32 v36, v36, v40
	v_mul_f32_e32 v37, v37, v41
	v_mul_f32_e32 v44, v44, v180
	v_mul_f32_e32 v41, v36, v37
	v_mul_f32_e32 v39, v35, v38
	v_mul_f32_e32 v184, v44, v37
	v_mov_b32_e32 v193, v41
	v_mul_f32_e32 v36, v102, v37
	v_mul_f32_e32 v40, v184, v192
	v_mul_f32_e32 v41, v185, v193
	v_mul_f32_e32 v38, v38, v36
	v_mul_f32_e32 v39, v39, v37
	v_cvt_pk_bf16_f32 v36, v40, v41
	v_cvt_pk_bf16_f32 v37, v38, v39
	v_cvt_pk_bf16_f32 v38, v42, v43
	v_cvt_pk_bf16_f32 v39, v46, v47
	ds_read_b64_tr_b16 v[40:41], v107 offset:61440
	ds_read_b64_tr_b16 v[42:43], v107 offset:61952
	v_mov_b32_e32 v191, v45
	ds_read_b64_tr_b16 v[44:45], v107 offset:62464
	ds_read_b64_tr_b16 v[46:47], v107 offset:62976
	s_waitcnt lgkmcnt(2)
	v_mfma_f32_32x32x16_bf16 v[0:15], v[36:39], v[40:43], v[0:15]
	ds_read_b64_tr_b16 v[40:41], v153 offset:63488
	ds_read_b64_tr_b16 v[42:43], v153 offset:64000
	v_mul_f32_e32 v186, v198, v181
	v_mul_f32_e32 v180, v199, v181
	v_mul_f32_e64 v184, v186, v190
	v_mul_f32_e64 v185, v187, v191
	v_mul_f32_e32 v182, v182, v180
	v_mul_f32_e32 v183, v183, v181
	v_cvt_pk_bf16_f32 v180, v184, v185
	ds_read_b64_tr_b16 v[184:185], v153 offset:64512
	ds_read_b64_tr_b16 v[186:187], v153 offset:65024
	s_waitcnt lgkmcnt(2)
	v_mfma_f32_32x32x16_bf16 v[16:31], v[36:39], v[40:43], v[16:31]
	v_cvt_pk_bf16_f32 v181, v182, v183
	v_cvt_pk_bf16_f32 v182, v188, v189
	v_cvt_pk_bf16_f32 v183, v196, v197
	s_nop 1
	v_mfma_f32_32x32x16_bf16 v[0:15], v[180:183], v[44:47], v[0:15]
	s_waitcnt lgkmcnt(0)
	v_mfma_f32_32x32x16_bf16 v[16:31], v[180:183], v[184:187], v[16:31]
	s_cbranch_vccnz .LBB0_389
	v_mul_f32_e32 v33, v33, v34
	v_mul_f32_e32 v32, v32, v33
	v_mul_f32_e32 v103, v103, v32
	s_sub_i32 s12, s12, 32
	s_add_i32 s17, s17, -1
	v_cmp_le_f32_e32 vcc, s28, v103
	s_cmp_eq_u64 vcc, 0
	s_cselect_b64 s[10:11], -1, 0
	s_andn2_b64 vcc, exec, s[10:11]
	s_cbranch_vccnz .LBB0_390

; #define LAS __attribute__((address_space(3)))
; #define LDS_WAIT() asm volatile("s_waitcnt lgkmcnt(0)" ::: "memory")
; __device__ __forceinline__ float max2f(float a, float b) { float r; asm("v_max_f32_e32 %0, %1, %2" : "=v"(r) : "v"(a), "v"(b)); return r; }
; __device__ __forceinline__ float pswap_max(float m) { auto rr = __builtin_amdgcn_permlane32_swap(__float_as_uint(m), __float_as_uint(m), false, false); return max2f(__uint_as_float(rr[0]), __uint_as_float(rr[1])); }
; __device__ __forceinline__ void rescale_o(f32x16 (&o)[2], float alpha, LAS float* wsf, int r32, int hi) {
;     if (hi == 0) wsf[r32] = alpha;
;     LDS_WAIT(); asm volatile("" ::: "memory");
; #pragma unroll
;     for (int j = 0; j < 4; ++j) { const f32x4 a = *(const LAS f32x4*)(wsf + 8 * j + 4 * hi);
; #pragma unroll
;         for (int e = 0; e < 4; ++e) { o[0][4 * j + e] *= a[e]; o[1][4 * j + e] *= a[e]; } }
;     LDS_WAIT(); asm volatile("" ::: "memory");
; __device__ __forceinline__ void fox_softmax(f32x16& p0, f32x16& p1, f32x16 (&o)[2], float& mrun, float& lrun, int kv0, int qtok, bool diag, LAS float* wsf, int r32, int hi) {
;     ...
;     float mt = pswap_max(rowmax32(p0, p1));
;     if (__any(mt > mrun + RESC_THR)) { const float mnew = max2f(mrun, mt), alpha = __builtin_amdgcn_exp2f(mrun - mnew); mrun = mnew; lrun *= alpha; rescale_o(o, alpha, wsf, r32, hi); }
.LBB0_428:
	v_max3_f32 v96, v80, v81, v32
	v_max3_f32 v98, v82, v83, v33
	s_nop 0
	v_max3_f32 v96, v96, v34, v35
	v_max3_f32 v98, v98, v86, v87
	s_nop 0
	v_max3_f32 v96, v96, v84, v85
	v_max3_f32 v98, v98, v38, v39
	s_nop 0
	v_max3_f32 v96, v96, v36, v37
	v_max3_f32 v98, v98, v90, v91
	s_nop 0
	v_max3_f32 v96, v96, v88, v89
	v_max3_f32 v98, v98, v42, v43
	s_nop 0
	v_max3_f32 v96, v96, v40, v41
	v_max3_f32 v98, v98, v94, v95
	s_nop 0
	v_max3_f32 v96, v96, v92, v93
	v_max3_f32 v98, v98, v46, v47
	s_nop 0
	v_max3_f32 v96, v96, v44, v45
	s_nop 0
	v_max_f32_e32 v96, v96, v98
	s_nop 0
	v_mov_b32_e32 v98, v96
	s_nop 1
	v_permlane32_swap_b32_e32 v96, v98
	v_max_f32_e32 v96, v96, v98
	v_add_f32_e32 v98, 0x41000000, v214
	v_cmp_gt_f32_e32 vcc, v96, v98
	s_cbranch_vccz .LBB0_432
	v_max_f32_e32 v96, v214, v96
	s_nop 0
	v_sub_f32_e32 v98, v214, v96
	v_exp_f32_e32 v98, v98
	s_and_saveexec_b64 s[6:7], s[4:5]
	ds_write_b32 v165, v98
	s_or_b64 exec, exec, s[6:7]
	s_waitcnt lgkmcnt(0)
	v_add_u32_e32 v99, s86, v166
	ds_read_b128 v[218:221], v99 offset:96
	ds_read_b128 v[222:225], v99 offset:64
	ds_read_b128 v[226:229], v99 offset:32
	ds_read_b128 v[230:233], v99
	s_waitcnt lgkmcnt(0)
	v_mul_f32_e32 v149, v149, v98
	s_waitcnt lgkmcnt(3)
	v_mul_f32_e32 v28, v28, v218
	v_mul_f32_e32 v29, v29, v219
	s_waitcnt lgkmcnt(2)
	v_mul_f32_e32 v24, v24, v222
	v_mul_f32_e32 v25, v25, v223
	s_waitcnt lgkmcnt(1)
	v_mul_f32_e32 v20, v20, v226
	v_mul_f32_e32 v21, v21, v227
	v_mul_f32_e32 v30, v30, v220
	v_mul_f32_e32 v31, v31, v221
	v_mul_f32_e32 v26, v26, v224
	v_mul_f32_e32 v27, v27, v225
	v_mul_f32_e32 v22, v22, v228
	v_mul_f32_e32 v23, v23, v229
	s_waitcnt lgkmcnt(0)
	v_mul_f32_e32 v18, v18, v232
	v_mul_f32_e32 v19, v19, v233
	v_mul_f32_e32 v16, v16, v230
	v_mul_f32_e32 v17, v17, v231
	v_mul_f32_e32 v12, v12, v218
	v_mul_f32_e32 v13, v13, v219
	v_mul_f32_e32 v8, v8, v222
	v_mul_f32_e32 v9, v9, v223
	v_mul_f32_e32 v4, v4, v226
	v_mul_f32_e32 v5, v5, v227
	v_mul_f32_e32 v14, v14, v220
	v_mul_f32_e32 v15, v15, v221
	v_mul_f32_e32 v10, v10, v224
	v_mul_f32_e32 v11, v11, v225
	v_mul_f32_e32 v6, v6, v228
	v_mul_f32_e32 v7, v7, v229
	v_mul_f32_e32 v2, v2, v232
	v_mul_f32_e32 v3, v3, v233
	v_mul_f32_e32 v0, v0, v230
	v_mul_f32_e32 v1, v1, v231
	v_mov_b32_e32 v214, v96
; #define LAS __attribute__((address_space(3)))
; #define ATT_PACK8(P, B) __builtin_bit_cast(bf16x8, (v4u){cvtpk(P[B], P[B + 1]), cvtpk(P[B + 2], P[B + 3]), cvtpk(P[B + 4], P[B + 5]), cvtpk(P[B + 6], P[B + 7])})
; __device__ __forceinline__ void fox_softmax(f32x16& p0, f32x16& p1, f32x16 (&o)[2], float& mrun, float& lrun, int kv0, int qtok, bool diag, LAS float* wsf, int r32, int hi) {
;     ...
;     float rs = 0.f;
; #pragma unroll
;     for (int r = 0; r < 16; ++r) { p0[r] = __builtin_amdgcn_exp2f(p0[r] - mrun); p1[r] = __builtin_amdgcn_exp2f(p1[r] - mrun); rs += p0[r] + p1[r]; }
;     lrun += rs;
; template <int TYPE>
; __device__ __forceinline__ void causal_wg_unit(const bf16* proj, const float* cum2, const float* gn, unsigned char* obuf, int b, int h, int qb, LAS unsigned char* kvbuf, LAS float* ncum, lptr wl, LAS float* wsf, int tid, int wave) {
;     ...
;             const bf16x8 pa0 = ATT_PACK8(pc0, 0), pa1 = ATT_PACK8(pc0, 8), pa2 = ATT_PACK8(pc1, 0), pa3 = ATT_PACK8(pc1, 8);
;             const LAS unsigned char* vb = kvbuf + (s % 3) * 16384 + vbo;
;             pv_step<4096>(o, vb, vsw, 0, pa0); pv_step<4096>(o, vb, vsw, 1, pa1); pv_step<4096>(o, vb, vsw, 2, pa2); pv_step<4096>(o, vb, vsw, 3, pa3);
.LBB0_432:
	v_sub_f32_e32 v32, v32, v214
	v_sub_f32_e32 v80, v80, v214
	v_exp_f32_e32 v217, v32
	v_sub_f32_e32 v32, v81, v214
	v_exp_f32_e32 v215, v80
	v_exp_f32_e32 v96, v32
	v_sub_f32_e32 v32, v33, v214
	v_exp_f32_e32 v80, v32
	v_add_f32_e32 v81, v217, v215
	s_mul_hi_u32 s6, s47, 0xaaaaaaab
	s_lshr_b32 s6, s6, 1
	v_add_f32_e32 v32, v80, v96
	v_add_f32_e32 v33, v81, v97
	s_mul_i32 s6, s6, 0xc000
	v_add_f32_e32 v99, v32, v33
	v_sub_f32_e32 v32, v82, v214
	v_exp_f32_e32 v81, v32
	v_sub_f32_e32 v32, v34, v214
	v_exp_f32_e32 v226, v32
	v_sub_f32_e32 v32, v83, v214
	v_exp_f32_e32 v98, v32
	v_sub_f32_e32 v32, v35, v214
	v_exp_f32_e32 v82, v32
	v_add_f32_e32 v83, v226, v81
	v_subrev_u32_e32 v231, s6, v192
	v_subrev_u32_e32 v232, s6, v193
	v_add_f32_e32 v32, v82, v98
	v_add_f32_e32 v33, v83, v99
	v_subrev_u32_e32 v236, s6, v198
	v_add_f32_e32 v35, v32, v33
	v_sub_f32_e32 v32, v84, v214
	v_exp_f32_e32 v83, v32
	v_sub_f32_e32 v32, v36, v214
	v_exp_f32_e32 v99, v32
	v_sub_f32_e32 v32, v85, v214
	v_exp_f32_e32 v34, v32
	v_sub_f32_e32 v32, v37, v214
	v_exp_f32_e32 v84, v32
	v_add_f32_e32 v85, v99, v83
	v_subrev_u32_e32 v237, s6, v199
	v_subrev_u32_e32 v229, s6, v190
	v_add_f32_e32 v32, v84, v34
	v_add_f32_e32 v33, v85, v35
	v_cvt_pk_bf16_f32 v34, v83, v34
	v_add_f32_e32 v37, v32, v33
	v_sub_f32_e32 v32, v86, v214
	v_exp_f32_e32 v35, v32
	v_sub_f32_e32 v32, v38, v214
	v_exp_f32_e32 v85, v32
	v_sub_f32_e32 v32, v87, v214
	v_exp_f32_e32 v36, v32
	v_sub_f32_e32 v32, v39, v214
	v_exp_f32_e32 v86, v32
	v_add_f32_e32 v87, v85, v35
	v_subrev_u32_e32 v38, s6, v201
	v_cvt_pk_bf16_f32 v35, v35, v36
	v_add_f32_e32 v32, v86, v36
	v_add_f32_e32 v33, v87, v37
	v_subrev_u32_e32 v37, s6, v200
	v_add_f32_e32 v219, v32, v33
	v_sub_f32_e32 v32, v88, v214
	v_exp_f32_e32 v87, v32
	v_sub_f32_e32 v32, v40, v214
	v_exp_f32_e32 v233, v32
	v_sub_f32_e32 v32, v89, v214
	v_exp_f32_e32 v218, v32
	v_sub_f32_e32 v32, v41, v214
	v_exp_f32_e32 v88, v32
	v_add_f32_e32 v89, v233, v87
	v_add3_u32 v36, s60, v38, v186
	v_add3_u32 v38, s60, v37, v186
	v_add_f32_e32 v32, v88, v218
	v_add_f32_e32 v33, v89, v219
	ds_read_b64_tr_b16 v[36:37], v36
	ds_read_b64_tr_b16 v[38:39], v38
	v_add_f32_e32 v221, v32, v33
	v_sub_f32_e32 v32, v90, v214
	v_exp_f32_e32 v89, v32
	v_sub_f32_e32 v32, v42, v214
	v_exp_f32_e32 v219, v32
	v_sub_f32_e32 v32, v91, v214
	v_exp_f32_e32 v220, v32
	v_sub_f32_e32 v32, v43, v214
	v_exp_f32_e32 v90, v32
	v_add_f32_e32 v91, v219, v89
	v_add3_u32 v40, s60, v232, v186
	v_add3_u32 v42, s60, v231, v186
	v_add_f32_e32 v32, v90, v220
	v_add_f32_e32 v33, v91, v221
	ds_read_b64_tr_b16 v[40:41], v40
	ds_read_b64_tr_b16 v[42:43], v42
	v_add_f32_e32 v223, v32, v33
	v_sub_f32_e32 v32, v92, v214
	v_exp_f32_e32 v91, v32
	v_sub_f32_e32 v32, v44, v214
	v_exp_f32_e32 v221, v32
	v_sub_f32_e32 v32, v93, v214
	v_exp_f32_e32 v222, v32
	v_sub_f32_e32 v32, v45, v214
	v_exp_f32_e32 v44, v32
	v_add_f32_e32 v45, v221, v91
	v_subrev_u32_e32 v230, s6, v191
	v_subrev_u32_e32 v83, s6, v197
	v_add_f32_e32 v32, v44, v222
	v_add_f32_e32 v33, v45, v223
	v_sub_f32_e32 v45, v94, v214
	v_add_f32_e32 v93, v32, v33
	v_cvt_pk_bf16_f32 v32, v215, v96
	v_cvt_pk_bf16_f32 v33, v81, v98
	v_exp_f32_e32 v45, v45
	v_subrev_u32_e32 v81, s6, v196
	s_waitcnt lgkmcnt(2)
	v_mfma_f32_32x32x16_bf16 v[16:31], v[32:35], v[36:39], v[16:31]
	v_sub_f32_e32 v36, v95, v214
	v_exp_f32_e32 v92, v36
	v_cvt_pk_bf16_f32 v36, v87, v218
	v_cvt_pk_bf16_f32 v37, v89, v220
	v_cvt_pk_bf16_f32 v38, v91, v222
	v_cvt_pk_bf16_f32 v39, v45, v92
	v_subrev_u32_e32 v227, s6, v188
	s_waitcnt lgkmcnt(0)
	v_mfma_f32_32x32x16_bf16 v[0:15], v[32:35], v[40:43], v[0:15]
	v_add3_u32 v32, s60, v237, v186
	v_add3_u32 v34, s60, v236, v186
	ds_read_b64_tr_b16 v[32:33], v32
	ds_read_b64_tr_b16 v[34:35], v34
	v_add3_u32 v40, s60, v230, v186
	v_add3_u32 v42, s60, v229, v186
	ds_read_b64_tr_b16 v[40:41], v40
	ds_read_b64_tr_b16 v[42:43], v42
	v_subrev_u32_e32 v228, s6, v189
	s_waitcnt lgkmcnt(2)
	v_mfma_f32_32x32x16_bf16 v[16:31], v[36:39], v[32:35], v[16:31]
	v_cvt_pk_bf16_f32 v32, v217, v80
	v_cvt_pk_bf16_f32 v33, v226, v82
	v_cvt_pk_bf16_f32 v34, v99, v84
	v_cvt_pk_bf16_f32 v35, v85, v86
	v_sub_f32_e32 v46, v46, v214
	v_exp_f32_e32 v80, v46
	v_subrev_u32_e32 v224, s6, v185
	s_waitcnt lgkmcnt(0)
	v_mfma_f32_32x32x16_bf16 v[0:15], v[36:39], v[40:43], v[0:15]
	v_add3_u32 v36, s60, v83, v186
	v_add3_u32 v38, s60, v81, v186
	ds_read_b64_tr_b16 v[36:37], v36
	ds_read_b64_tr_b16 v[38:39], v38
	v_add3_u32 v40, s60, v228, v186
	v_add3_u32 v42, s60, v227, v186
	ds_read_b64_tr_b16 v[40:41], v40
	ds_read_b64_tr_b16 v[42:43], v42
	v_subrev_u32_e32 v225, s6, v187
	s_waitcnt lgkmcnt(2)
	v_mfma_f32_32x32x16_bf16 v[16:31], v[32:35], v[36:39], v[16:31]
	v_sub_f32_e32 v36, v47, v214
	v_exp_f32_e32 v46, v36
	v_subrev_u32_e32 v234, s6, v194
	v_subrev_u32_e32 v235, s6, v195
	v_cvt_pk_bf16_f32 v36, v233, v88
	v_cvt_pk_bf16_f32 v37, v219, v90
	v_cvt_pk_bf16_f32 v38, v221, v44
	s_waitcnt lgkmcnt(0)
	v_mfma_f32_32x32x16_bf16 v[0:15], v[32:35], v[40:43], v[0:15]
	v_add3_u32 v32, s60, v235, v186
	v_add3_u32 v34, s60, v234, v186
	v_add3_u32 v40, s60, v225, v186
	v_add3_u32 v42, s60, v224, v186
	v_cvt_pk_bf16_f32 v39, v80, v46
	ds_read_b64_tr_b16 v[32:33], v32
	ds_read_b64_tr_b16 v[34:35], v34
	ds_read_b64_tr_b16 v[40:41], v40
	ds_read_b64_tr_b16 v[42:43], v42
	s_waitcnt lgkmcnt(2)
	v_mfma_f32_32x32x16_bf16 v[16:31], v[36:39], v[32:35], v[16:31]
	v_add_f32_e32 v47, v80, v45
	v_add_f32_e64 v32, v46, v92
	v_add_f32_e64 v33, v47, v93
	v_add_f32_e32 v32, v32, v33
	v_add_f32_e32 v149, v149, v32
	s_waitcnt lgkmcnt(0)
	v_mfma_f32_32x32x16_bf16 v[0:15], v[36:39], v[40:43], v[0:15]
	s_andn2_b64 vcc, exec, s[42:43]
	s_cbranch_vccz .LBB0_420
	s_branch .LBB0_421

; #define LAS __attribute__((address_space(3)))
; #define LDS_WAIT() asm volatile("s_waitcnt lgkmcnt(0)" ::: "memory")
; __device__ __forceinline__ float max2f(float a, float b) { float r; asm("v_max_f32_e32 %0, %1, %2" : "=v"(r) : "v"(a), "v"(b)); return r; }
; __device__ __forceinline__ float pswap_max(float m) { auto rr = __builtin_amdgcn_permlane32_swap(__float_as_uint(m), __float_as_uint(m), false, false); return max2f(__uint_as_float(rr[0]), __uint_as_float(rr[1])); }
; __device__ __forceinline__ void rescale_o(f32x16 (&o)[2], float alpha, LAS float* wsf, int r32, int hi) {
;     if (hi == 0) wsf[r32] = alpha;
;     LDS_WAIT(); asm volatile("" ::: "memory");
; #pragma unroll
;     for (int j = 0; j < 4; ++j) { const f32x4 a = *(const LAS f32x4*)(wsf + 8 * j + 4 * hi);
; #pragma unroll
;         for (int e = 0; e < 4; ++e) { o[0][4 * j + e] *= a[e]; o[1][4 * j + e] *= a[e]; } }
;     LDS_WAIT(); asm volatile("" ::: "memory");
; __device__ __forceinline__ void fox_softmax(f32x16& p0, f32x16& p1, f32x16 (&o)[2], float& mrun, float& lrun, int kv0, int qtok, bool diag, LAS float* wsf, int r32, int hi) {
;     ...
;     float mt = pswap_max(rowmax32(p0, p1));
;     if (__any(mt > mrun + RESC_THR)) { const float mnew = max2f(mrun, mt), alpha = __builtin_amdgcn_exp2f(mrun - mnew); mrun = mnew; lrun *= alpha; rescale_o(o, alpha, wsf, r32, hi); }
.LBB0_1338:
	v_max3_f32 v96, v80, v81, v32
	v_max3_f32 v98, v82, v83, v33
	s_nop 0
	v_max3_f32 v96, v96, v34, v35
	v_max3_f32 v98, v98, v86, v87
	s_nop 0
	v_max3_f32 v96, v96, v84, v85
	v_max3_f32 v98, v98, v38, v39
	s_nop 0
	v_max3_f32 v96, v96, v36, v37
	v_max3_f32 v98, v98, v90, v91
	s_nop 0
	v_max3_f32 v96, v96, v88, v89
	v_max3_f32 v98, v98, v42, v43
	s_nop 0
	v_max3_f32 v96, v96, v40, v41
	v_max3_f32 v98, v98, v94, v95
	s_nop 0
	v_max3_f32 v96, v96, v92, v93
	v_max3_f32 v98, v98, v46, v47
	s_nop 0
	v_max3_f32 v96, v96, v44, v45
	s_nop 0
	v_max_f32_e32 v96, v96, v98
	s_nop 0
	v_mov_b32_e32 v98, v96
	s_nop 1
	v_permlane32_swap_b32_e32 v96, v98
	v_max_f32_e32 v96, v96, v98
	v_add_f32_e32 v98, 0x41000000, v214
	v_cmp_gt_f32_e32 vcc, v96, v98
	s_cbranch_vccz .LBB0_1342
	v_max_f32_e32 v96, v214, v96
	s_nop 0
	v_sub_f32_e32 v98, v214, v96
	v_exp_f32_e32 v98, v98
	s_and_saveexec_b64 s[6:7], s[4:5]
	ds_write_b32 v165, v98
	s_or_b64 exec, exec, s[6:7]
	s_waitcnt lgkmcnt(0)
	v_add_u32_e32 v99, s82, v166
	ds_read_b128 v[218:221], v99 offset:96
	ds_read_b128 v[222:225], v99 offset:64
	ds_read_b128 v[226:229], v99 offset:32
	ds_read_b128 v[230:233], v99
	s_waitcnt lgkmcnt(0)
	v_mul_f32_e32 v149, v149, v98
	s_waitcnt lgkmcnt(3)
	v_mul_f32_e32 v28, v28, v218
	v_mul_f32_e32 v29, v29, v219
	s_waitcnt lgkmcnt(2)
	v_mul_f32_e32 v24, v24, v222
	v_mul_f32_e32 v25, v25, v223
	s_waitcnt lgkmcnt(1)
	v_mul_f32_e32 v20, v20, v226
	v_mul_f32_e32 v21, v21, v227
	v_mul_f32_e32 v30, v30, v220
	v_mul_f32_e32 v31, v31, v221
	v_mul_f32_e32 v26, v26, v224
	v_mul_f32_e32 v27, v27, v225
	v_mul_f32_e32 v22, v22, v228
	v_mul_f32_e32 v23, v23, v229
	s_waitcnt lgkmcnt(0)
	v_mul_f32_e32 v18, v18, v232
	v_mul_f32_e32 v19, v19, v233
	v_mul_f32_e32 v16, v16, v230
	v_mul_f32_e32 v17, v17, v231
	v_mul_f32_e32 v12, v12, v218
	v_mul_f32_e32 v13, v13, v219
	v_mul_f32_e32 v8, v8, v222
	v_mul_f32_e32 v9, v9, v223
	v_mul_f32_e32 v4, v4, v226
	v_mul_f32_e32 v5, v5, v227
	v_mul_f32_e32 v14, v14, v220
	v_mul_f32_e32 v15, v15, v221
	v_mul_f32_e32 v10, v10, v224
	v_mul_f32_e32 v11, v11, v225
	v_mul_f32_e32 v6, v6, v228
	v_mul_f32_e32 v7, v7, v229
	v_mul_f32_e32 v2, v2, v232
	v_mul_f32_e32 v3, v3, v233
	v_mul_f32_e32 v0, v0, v230
	v_mul_f32_e32 v1, v1, v231
	v_mov_b32_e32 v214, v96
